# speedup vs baseline: 1.0191x; 1.0023x over previous
.LBB3_2:
	v_pk_mul_f32 v[4:5], v[92:93], v[34:35]
	s_xor_b64 s[12:13], s[0:1], -1
	v_exp_f32_e32 v6, v5
	v_exp_f32_e32 v7, v4
	v_pk_mul_f32 v[4:5], v[34:35], v[18:19]
	s_nop 0
	v_fma_f32 v5, v48, v6, v5
	v_fmac_f32_e32 v4, v7, v5
	v_pk_fma_f32 v[2:3], v[2:3], v[4:5], v[78:79]
	v_lshl_add_u32 v4, v149, 1, v148
	v_cvt_pk_f16_f32 v2, v2, v3
	v_cvt_pk_f16_f32 v5, v122, v123
	v_cvt_pk_f16_f32 v3, v36, v37
	v_cvt_pk_f16_f32 v6, v38, v39
	ds_write_b16 v4, v2
	ds_write_b16_d16_hi v4, v2 offset:32
	ds_write_b16 v4, v5 offset:64
	ds_write_b16_d16_hi v4, v5 offset:96
	ds_write_b16 v4, v3 offset:128
	ds_write_b16_d16_hi v4, v3 offset:160
	ds_write_b16 v4, v6 offset:192
	ds_write_b16_d16_hi v4, v6 offset:224
	v_cvt_pk_f16_f32 v2, v40, v41
	v_cvt_pk_f16_f32 v5, v42, v43
	v_cvt_pk_f16_f32 v3, v44, v45
	v_cvt_pk_f16_f32 v6, v46, v47
	ds_write_b16 v4, v2 offset:256
	ds_write_b16_d16_hi v4, v2 offset:288
	ds_write_b16 v4, v5 offset:320
	ds_write_b16_d16_hi v4, v5 offset:352
	ds_write_b16 v4, v3 offset:384
	ds_write_b16_d16_hi v4, v3 offset:416
	ds_write_b16 v4, v6 offset:448
	ds_write_b16_d16_hi v4, v6 offset:480
	v_mov_b64_e32 v[80:81], v[60:61]
	v_mov_b64_e32 v[76:77], v[64:65]
	s_mov_b32 s3, 8
	s_mov_b64 s[0:1], 0
	s_andn2_b64 vcc, exec, s[12:13]
	v_mov_b64_e32 v[78:79], v[58:59]
	v_mov_b64_e32 v[74:75], v[62:63]
	v_mov_b32_e32 v151, v145
	v_mov_b32_e32 v150, v146
	s_cbranch_vccz .LBB3_10
